# norm/combine row loops: loop-invariant gain/scale/shift/gate vector loads hoisted out of the per-row loops into free VGPRs
# speedup vs baseline: 1.0236x; 1.0028x over previous
.LBB0_121:
	v_ashrrev_i32_e32 v1, 31, v0
	s_waitcnt lgkmcnt(0)
	v_lshlrev_b64 v[2:3], 4, v[0:1]
	s_load_dwordx2 s[0:1], s[6:7], 0x20
	s_load_dwordx2 s[8:9], s[6:7], 0x118
	s_load_dwordx2 s[10:11], s[6:7], 0x0
	v_lshl_add_u64 v[18:19], s[4:5], 0, v[2:3]
	s_mov_b64 s[4:5], 0x3000
	v_lshl_add_u64 v[24:25], v[18:19], 0, s[4:5]
	s_mov_b64 s[4:5], 0x3400
	v_lshl_add_u64 v[30:31], v[18:19], 0, s[4:5]
	s_mov_b64 s[4:5], 0x3800
	s_waitcnt lgkmcnt(0)
	v_lshl_add_u64 v[16:17], s[0:1], 0, v[2:3]
	s_mov_b64 s[0:1], 0x2000
	v_lshl_add_u64 v[36:37], v[18:19], 0, s[4:5]
	s_mov_b64 s[4:5], 0x3c00
	s_ashr_i32 s57, s56, 31
	v_lshl_add_u64 v[20:21], v[18:19], 0, s[0:1]
	s_mov_b64 s[0:1], 0x1000
	v_lshl_add_u64 v[42:43], v[18:19], 0, s[4:5]
	s_lshl_b64 s[4:5], s[56:57], 13
	v_lshl_add_u64 v[22:23], v[16:17], 0, s[0:1]
	v_lshl_add_u64 v[26:27], v[18:19], 0, s[0:1]
	s_mov_b64 s[0:1], 0x1400
	s_add_u32 s4, s10, s4
	v_lshl_add_u64 v[28:29], v[16:17], 0, s[0:1]
	v_lshl_add_u64 v[32:33], v[18:19], 0, s[0:1]
	s_mov_b64 s[0:1], 0x1800
	s_addc_u32 s5, s11, s5
	v_lshl_add_u64 v[34:35], v[16:17], 0, s[0:1]
	v_lshl_add_u64 v[38:39], v[18:19], 0, s[0:1]
	s_mov_b64 s[0:1], 0x1c00
	v_lshl_add_u64 v[2:3], s[4:5], 0, v[2:3]
	s_ashr_i32 s59, s58, 31
	v_lshl_add_u64 v[40:41], v[16:17], 0, s[0:1]
	v_lshl_add_u64 v[44:45], v[18:19], 0, s[0:1]
	v_lshl_add_u64 v[46:47], v[2:3], 0, s[0:1]
	s_lshl_b64 s[4:5], s[58:59], 13
	s_lshl_b64 s[0:1], s[56:57], 12
	s_add_u32 s0, s8, s0
	s_addc_u32 s1, s9, s1
	v_lshl_add_u64 v[0:1], v[0:1], 3, s[0:1]
	s_mov_b64 s[0:1], 0x800
	v_lshl_add_u64 v[48:49], v[0:1], 0, s[0:1]
	s_lshl_b64 s[6:7], s[58:59], 12
	v_mov_b32_e32 v50, 0x358637bd
	s_mov_b32 s0, 0x800000
	s_mov_b32 s1, s56
	global_load_dwordx4 v[212:215], v[20:21], off
	global_load_dwordx4 v[208:211], v[16:17], off
	global_load_dwordx4 v[204:207], v[18:19], off
	global_load_dwordx4 v[200:203], v[16:17], off offset:1024
	global_load_dwordx4 v[196:199], v[20:21], off offset:1024
	global_load_dwordx4 v[192:195], v[18:19], off offset:1024
	global_load_dwordx4 v[188:191], v[16:17], off offset:2048
	global_load_dwordx4 v[184:187], v[20:21], off offset:2048
	global_load_dwordx4 v[180:183], v[18:19], off offset:2048
	global_load_dwordx4 v[176:179], v[16:17], off offset:3072
	global_load_dwordx4 v[172:175], v[20:21], off offset:3072
	global_load_dwordx4 v[168:171], v[18:19], off offset:3072
	global_load_dwordx4 v[164:167], v[22:23], off
	global_load_dwordx4 v[160:163], v[24:25], off
	global_load_dwordx4 v[156:159], v[26:27], off
	global_load_dwordx4 v[152:155], v[28:29], off
	global_load_dwordx4 v[148:151], v[30:31], off
	global_load_dwordx4 v[140:143], v[32:33], off
	global_load_dwordx4 v[136:139], v[34:35], off
	global_load_dwordx4 v[132:135], v[36:37], off
	global_load_dwordx4 v[128:131], v[38:39], off
	global_load_dwordx4 v[124:127], v[40:41], off
	global_load_dwordx4 v[120:123], v[42:43], off
	global_load_dwordx4 v[116:119], v[44:45], off
.LBB0_122:
	global_load_dwordx4 v[12:15], v[46:47], off offset:-3072
	global_load_dwordx4 v[8:11], v[46:47], off offset:-2048
	global_load_dwordx4 v[0:3], v[46:47], off
	global_load_dwordx4 v[4:7], v[46:47], off offset:-1024
	v_add_co_u32_e32 v68, vcc, 0xfffff000, v46
	v_mov_b32_e32 v51, v144
	s_nop 0
	v_addc_co_u32_e32 v69, vcc, -1, v47, vcc
	global_load_dwordx4 v[52:55], v[68:69], off offset:-3072
	global_load_dwordx4 v[56:59], v[68:69], off offset:-2048
	global_load_dwordx4 v[60:63], v[68:69], off offset:-1024
	global_load_dwordx4 v[64:67], v[46:47], off offset:-4096
	v_lshlrev_b32_e32 v51, 2, v51
	v_xor_b32_e32 v103, 4, v51
	v_xor_b32_e32 v104, 8, v51
	v_xor_b32_e32 v105, 16, v51
	v_xor_b32_e32 v106, 32, v51
	v_xor_b32_e32 v107, 64, v51
	v_xor_b32_e32 v51, 0x80, v51
	s_add_i32 s1, s1, s58
	s_cmpk_lt_i32 s1, 0x2000
	v_lshl_add_u64 v[46:47], v[46:47], 0, s[4:5]
	s_waitcnt vmcnt(7)
	v_mul_f32_e32 v108, v12, v12
	s_waitcnt vmcnt(6)
	v_pk_mul_f32 v[80:81], v[10:11], v[10:11]
	v_pk_mul_f32 v[82:83], v[8:9], v[8:9]
	s_waitcnt vmcnt(4)
	v_mul_f32_e32 v84, v5, v5
	v_mul_f32_e32 v86, v7, v7
	v_mul_f32_e32 v101, v2, v2
	v_mul_f32_e32 v114, v3, v3
	v_pk_mov_b32 v[88:89], v[82:83], v[80:81] op_sel:[1,0]
	v_mov_b32_e32 v83, v81
	v_pk_fma_f32 v[80:81], v[4:5], v[4:5], v[84:85] op_sel_hi:[1,1,0]
	v_pk_fma_f32 v[84:85], v[6:7], v[6:7], v[86:87] op_sel_hi:[1,1,0]
	s_waitcnt vmcnt(3)
	v_mov_b32_e32 v90, v53
	s_waitcnt vmcnt(2)
	v_mov_b32_e32 v91, v57
	v_mov_b32_e32 v94, v55
	v_mov_b32_e32 v95, v59
	v_mov_b32_e32 v86, v52
	v_mov_b32_e32 v87, v56
	v_mov_b32_e32 v92, v54
	v_mov_b32_e32 v93, v58
	s_waitcnt vmcnt(1)
	v_pk_mul_f32 v[96:97], v[62:63], v[62:63]
	v_pk_mul_f32 v[98:99], v[60:61], v[60:61]
	v_pk_add_f32 v[82:83], v[88:89], v[82:83]
	v_mov_b32_e32 v81, v101
	v_mov_b32_e32 v85, v114
	v_pk_mul_f32 v[88:89], v[90:91], v[90:91]
	v_pk_mul_f32 v[90:91], v[94:95], v[94:95]
	v_pk_mov_b32 v[94:95], v[98:99], v[96:97] op_sel:[1,0]
	v_mov_b32_e32 v99, v97
	v_pk_add_f32 v[80:81], v[80:81], v[84:85]
	v_pk_fma_f32 v[84:85], v[86:87], v[86:87], v[88:89]
	v_pk_fma_f32 v[86:87], v[92:93], v[92:93], v[90:91]
	s_waitcnt vmcnt(0)
	v_mul_f32_e32 v100, v65, v65
	v_mul_f32_e32 v102, v67, v67
	v_pk_add_f32 v[88:89], v[94:95], v[98:99]
	v_pk_add_f32 v[84:85], v[84:85], v[86:87]
	v_mul_f32_e32 v109, v13, v13
	v_mul_f32_e32 v110, v14, v14
	v_mul_f32_e32 v111, v15, v15
	v_pk_fma_f32 v[96:97], v[64:65], v[64:65], v[100:101] op_sel_hi:[1,1,0]
	v_pk_fma_f32 v[100:101], v[66:67], v[66:67], v[102:103] op_sel_hi:[1,1,0]
	v_pk_add_f32 v[86:87], v[88:89], v[88:89] op_sel:[0,1] op_sel_hi:[1,0]
	v_pk_add_f32 v[84:85], v[84:85], v[84:85] op_sel:[0,1] op_sel_hi:[1,0]
	v_mov_b32_e32 v97, v110
	v_mov_b32_e32 v101, v111
	v_mov_b32_e32 v87, v109
	v_mov_b32_e32 v85, v108
	v_pk_add_f32 v[88:89], v[96:97], v[100:101]
	v_pk_add_f32 v[84:85], v[84:85], v[86:87]
	v_mul_f32_e32 v112, v0, v0
	v_pk_add_f32 v[84:85], v[84:85], v[88:89]
	v_mul_f32_e32 v113, v1, v1
	v_pk_add_f32 v[82:83], v[82:83], v[82:83] op_sel:[0,1] op_sel_hi:[1,0]
	v_pk_add_f32 v[84:85], v[84:85], v[84:85] op_sel:[0,1] op_sel_hi:[1,0]
	v_mov_b32_e32 v83, v113
	v_mov_b32_e32 v85, v112
	v_pk_add_f32 v[82:83], v[84:85], v[82:83]
	v_pk_add_f32 v[68:69], v[212:213], 1.0 op_sel_hi:[1,0]
	v_pk_add_f32 v[80:81], v[82:83], v[80:81]
	v_pk_add_f32 v[70:71], v[214:215], 1.0 op_sel_hi:[1,0]
	v_add_f32_e32 v80, v80, v81
	ds_bpermute_b32 v81, v103, v80
	s_waitcnt lgkmcnt(0)
	v_add_f32_e32 v80, v80, v81
	ds_bpermute_b32 v81, v104, v80
	s_waitcnt lgkmcnt(0)
	v_add_f32_e32 v80, v80, v81
	ds_bpermute_b32 v81, v105, v80
	s_waitcnt lgkmcnt(0)
	v_add_f32_e32 v80, v80, v81
	ds_bpermute_b32 v81, v106, v80
	s_waitcnt lgkmcnt(0)
	v_add_f32_e32 v80, v80, v81
	ds_bpermute_b32 v81, v107, v80
	s_waitcnt lgkmcnt(0)
	v_add_f32_e32 v80, v80, v81
	ds_bpermute_b32 v51, v51, v80
	s_waitcnt lgkmcnt(0)
	v_add_f32_e32 v51, v80, v51
	v_fmamk_f32 v51, v51, 0x3a000000, v50
	v_mul_f32_e32 v80, 0x4b800000, v51
	v_cmp_gt_f32_e32 vcc, s0, v51
	s_nop 1
	v_cndmask_b32_e32 v51, v51, v80, vcc
	v_rsq_f32_e32 v51, v51
	s_nop 0
	v_mul_f32_e32 v80, 0x45800000, v51
	v_cndmask_b32_e32 v80, v51, v80, vcc
	v_pk_mul_f32 v[52:53], v[52:53], v[80:81] op_sel_hi:[1,0]
	v_pk_mul_f32 v[54:55], v[54:55], v[80:81] op_sel_hi:[1,0]
	v_pk_mul_f32 v[52:53], v[208:209], v[52:53]
	v_pk_mul_f32 v[54:55], v[210:211], v[54:55]
	v_pk_fma_f32 v[52:53], v[68:69], v[52:53], v[204:205]
	v_pk_fma_f32 v[54:55], v[70:71], v[54:55], v[206:207]
	v_cvt_pk_bf16_f32 v52, v52, v53
	v_cvt_pk_bf16_f32 v53, v54, v55
	global_store_dwordx2 v[48:49], v[52:53], off offset:-2048
	s_nop 0
	v_pk_mul_f32 v[56:57], v[56:57], v[80:81] op_sel_hi:[1,0]
	v_pk_mul_f32 v[58:59], v[58:59], v[80:81] op_sel_hi:[1,0]
	v_pk_mul_f32 v[60:61], v[60:61], v[80:81] op_sel_hi:[1,0]
	v_pk_mul_f32 v[62:63], v[62:63], v[80:81] op_sel_hi:[1,0]
	v_pk_mul_f32 v[64:65], v[64:65], v[80:81] op_sel_hi:[1,0]
	v_pk_mul_f32 v[66:67], v[66:67], v[80:81] op_sel_hi:[1,0]
	v_pk_mul_f32 v[12:13], v[12:13], v[80:81] op_sel_hi:[1,0]
	v_pk_mul_f32 v[14:15], v[14:15], v[80:81] op_sel_hi:[1,0]
	v_pk_mul_f32 v[8:9], v[8:9], v[80:81] op_sel_hi:[1,0]
	v_pk_mul_f32 v[10:11], v[10:11], v[80:81] op_sel_hi:[1,0]
	v_pk_mul_f32 v[4:5], v[4:5], v[80:81] op_sel_hi:[1,0]
	v_pk_mul_f32 v[6:7], v[6:7], v[80:81] op_sel_hi:[1,0]
	v_pk_mul_f32 v[0:1], v[0:1], v[80:81] op_sel_hi:[1,0]
	v_pk_mul_f32 v[2:3], v[2:3], v[80:81] op_sel_hi:[1,0]
	v_pk_mul_f32 v[52:53], v[200:201], v[56:57]
	v_pk_add_f32 v[56:57], v[196:197], 1.0 op_sel_hi:[1,0]
	v_pk_mul_f32 v[54:55], v[202:203], v[58:59]
	v_pk_add_f32 v[58:59], v[198:199], 1.0 op_sel_hi:[1,0]
	v_pk_fma_f32 v[52:53], v[56:57], v[52:53], v[192:193]
	v_pk_fma_f32 v[54:55], v[58:59], v[54:55], v[194:195]
	v_cvt_pk_bf16_f32 v52, v52, v53
	v_cvt_pk_bf16_f32 v53, v54, v55
	global_store_dwordx2 v[48:49], v[52:53], off offset:-1536
	s_nop 0
	v_pk_mul_f32 v[52:53], v[188:189], v[60:61]
	v_pk_add_f32 v[56:57], v[184:185], 1.0 op_sel_hi:[1,0]
	v_pk_mul_f32 v[54:55], v[190:191], v[62:63]
	v_pk_add_f32 v[58:59], v[186:187], 1.0 op_sel_hi:[1,0]
	v_pk_fma_f32 v[52:53], v[56:57], v[52:53], v[180:181]
	v_pk_fma_f32 v[54:55], v[58:59], v[54:55], v[182:183]
	v_cvt_pk_bf16_f32 v52, v52, v53
	v_cvt_pk_bf16_f32 v53, v54, v55
	global_store_dwordx2 v[48:49], v[52:53], off offset:-1024
	s_nop 0
	v_pk_mul_f32 v[52:53], v[64:65], v[176:177]
	v_pk_add_f32 v[56:57], v[172:173], 1.0 op_sel_hi:[1,0]
	v_pk_mul_f32 v[54:55], v[66:67], v[178:179]
	v_pk_add_f32 v[58:59], v[174:175], 1.0 op_sel_hi:[1,0]
	v_pk_fma_f32 v[52:53], v[52:53], v[56:57], v[168:169]
	v_pk_fma_f32 v[54:55], v[54:55], v[58:59], v[170:171]
	v_cvt_pk_bf16_f32 v52, v52, v53
	v_cvt_pk_bf16_f32 v53, v54, v55
	global_store_dwordx2 v[48:49], v[52:53], off offset:-512
	s_nop 0
	v_pk_mul_f32 v[12:13], v[12:13], v[164:165]
	v_pk_add_f32 v[52:53], v[160:161], 1.0 op_sel_hi:[1,0]
	v_pk_mul_f32 v[14:15], v[14:15], v[166:167]
	v_pk_add_f32 v[54:55], v[162:163], 1.0 op_sel_hi:[1,0]
	v_pk_fma_f32 v[12:13], v[12:13], v[52:53], v[156:157]
	v_pk_fma_f32 v[14:15], v[14:15], v[54:55], v[158:159]
	v_cvt_pk_bf16_f32 v12, v12, v13
	v_cvt_pk_bf16_f32 v13, v14, v15
	global_store_dwordx2 v[48:49], v[12:13], off
	s_nop 0
	v_pk_mul_f32 v[8:9], v[8:9], v[152:153]
	v_pk_add_f32 v[12:13], v[148:149], 1.0 op_sel_hi:[1,0]
	v_pk_mul_f32 v[10:11], v[10:11], v[154:155]
	v_pk_add_f32 v[14:15], v[150:151], 1.0 op_sel_hi:[1,0]
	v_pk_fma_f32 v[8:9], v[8:9], v[12:13], v[140:141]
	v_pk_fma_f32 v[10:11], v[10:11], v[14:15], v[142:143]
	v_cvt_pk_bf16_f32 v8, v8, v9
	v_cvt_pk_bf16_f32 v9, v10, v11
	global_store_dwordx2 v[48:49], v[8:9], off offset:512
	s_nop 0
	v_pk_mul_f32 v[4:5], v[4:5], v[136:137]
	v_pk_add_f32 v[8:9], v[132:133], 1.0 op_sel_hi:[1,0]
	v_pk_mul_f32 v[6:7], v[6:7], v[138:139]
	v_pk_add_f32 v[10:11], v[134:135], 1.0 op_sel_hi:[1,0]
	v_pk_fma_f32 v[4:5], v[4:5], v[8:9], v[128:129]
	v_pk_fma_f32 v[6:7], v[6:7], v[10:11], v[130:131]
	v_cvt_pk_bf16_f32 v4, v4, v5
	v_cvt_pk_bf16_f32 v5, v6, v7
	global_store_dwordx2 v[48:49], v[4:5], off offset:1024
	s_nop 0
	v_pk_mul_f32 v[0:1], v[0:1], v[124:125]
	v_pk_add_f32 v[4:5], v[120:121], 1.0 op_sel_hi:[1,0]
	v_pk_mul_f32 v[2:3], v[2:3], v[126:127]
	v_pk_add_f32 v[6:7], v[122:123], 1.0 op_sel_hi:[1,0]
	v_pk_fma_f32 v[0:1], v[0:1], v[4:5], v[116:117]
	v_pk_fma_f32 v[2:3], v[2:3], v[6:7], v[118:119]
	v_cvt_pk_bf16_f32 v0, v0, v1
	v_cvt_pk_bf16_f32 v1, v2, v3
	global_store_dwordx2 v[48:49], v[0:1], off offset:1536
	v_lshl_add_u64 v[48:49], v[48:49], 0, s[6:7]
	s_cbranch_scc1 .LBB0_122

.LBB0_1508:
	v_readlane_b32 s0, v247, 25
	v_readlane_b32 s1, v247, 26
	s_and_b64 vcc, exec, s[0:1]
	s_cbranch_vccnz .LBB0_1511
	v_ashrrev_i32_e32 v53, 31, v52
	s_load_dwordx2 s[4:5], s[10:11], 0x0
	s_load_dwordx2 s[0:1], s[10:11], 0x20
	s_load_dwordx4 s[12:15], s[10:11], 0x190
	s_load_dwordx2 s[6:7], s[10:11], 0x1c8
	s_load_dwordx4 s[16:19], s[10:11], 0x118
	s_load_dwordx2 s[8:9], s[10:11], 0x130
	s_waitcnt lgkmcnt(0)
	v_lshlrev_b64 v[0:1], 4, v[52:53]
	v_lshl_add_u64 v[4:5], s[0:1], 0, v[0:1]
	s_mov_b64 s[0:1], 0x2000
	v_lshl_add_u64 v[2:3], s[20:21], 0, v[0:1]
	v_lshl_add_u64 v[68:69], v[4:5], 0, s[0:1]
	s_mov_b64 s[0:1], 0xe000
	v_lshl_add_u64 v[70:71], v[2:3], 0, s[0:1]
	s_mov_b64 s[0:1], 0xc000
	v_lshl_add_u64 v[72:73], v[2:3], 0, s[0:1]
	s_mov_b64 s[0:1], 0x3000
	v_lshl_add_u64 v[74:75], v[4:5], 0, s[0:1]
	s_mov_b64 s[0:1], 0xf000
	v_lshl_add_u64 v[76:77], v[2:3], 0, s[0:1]
	s_mov_b64 s[0:1], 0xd000
	v_lshl_add_u64 v[78:79], v[2:3], 0, s[0:1]
	s_mov_b64 s[0:1], 0x3400
	v_lshl_add_u64 v[80:81], v[4:5], 0, s[0:1]
	s_mov_b64 s[0:1], 0xf400
	v_lshl_add_u64 v[82:83], v[2:3], 0, s[0:1]
	s_mov_b64 s[0:1], 0xd400
	v_lshl_add_u64 v[84:85], v[2:3], 0, s[0:1]
	s_mov_b64 s[0:1], 0x3800
	v_lshlrev_b64 v[54:55], 3, v[52:53]
	v_lshl_add_u64 v[86:87], v[4:5], 0, s[0:1]
	s_mov_b64 s[0:1], 0xf800
	v_lshl_add_u64 v[56:57], s[6:7], 0, v[54:55]
	s_mov_b64 s[6:7], 0xa000
	v_lshl_add_u64 v[88:89], v[2:3], 0, s[0:1]
	s_mov_b64 s[0:1], 0xd800
	v_lshl_add_u64 v[58:59], v[2:3], 0, s[6:7]
	s_mov_b64 s[6:7], 0xb000
	v_lshl_add_u64 v[90:91], v[2:3], 0, s[0:1]
	s_mov_b64 s[0:1], 0x3c00
	v_lshl_add_u64 v[60:61], v[2:3], 0, s[6:7]
	s_mov_b64 s[6:7], 0xb400
	v_lshl_add_u64 v[92:93], v[4:5], 0, s[0:1]
	s_mov_b64 s[0:1], 0xfc00
	v_lshl_add_u64 v[62:63], v[2:3], 0, s[6:7]
	s_mov_b64 s[6:7], 0xb800
	v_lshl_add_u64 v[94:95], v[2:3], 0, s[0:1]
	s_mov_b64 s[0:1], 0xdc00
	v_lshl_add_u64 v[64:65], v[2:3], 0, s[6:7]
	s_mov_b64 s[6:7], 0xbc00
	v_lshl_add_u64 v[96:97], v[2:3], 0, s[0:1]
	s_lshl_b32 s0, s2, 4
	s_lshl_b32 s1, s33, 1
	s_ashr_i32 s57, s56, 31
	v_lshl_add_u64 v[66:67], v[2:3], 0, s[6:7]
	s_add_i32 s20, s0, s1
	s_lshl_b32 s0, s3, 4
	s_lshl_b64 s[6:7], s[56:57], 13
	s_add_u32 s4, s4, s6
	s_addc_u32 s5, s5, s7
	v_lshl_add_u64 v[0:1], s[4:5], 0, v[0:1]
	s_mov_b64 s[4:5], 0x1c00
	s_ashr_i32 s59, s58, 31
	v_lshl_add_u64 v[98:99], v[0:1], 0, s[4:5]
	s_lshl_b64 s[22:23], s[58:59], 13
	s_lshl_b64 s[4:5], s[56:57], 12
	s_add_u32 s24, s8, s4
	s_addc_u32 s25, s9, s5
	s_lshl_b64 s[26:27], s[58:59], 12
	s_add_u32 s16, s16, s4
	s_addc_u32 s17, s17, s5
	s_add_u32 s18, s18, s4
	s_addc_u32 s19, s19, s5
	v_mov_b32_e32 v53, 0
	v_mov_b32_e32 v108, 0x358637bd
	s_mov_b32 s1, 0x800000
	s_mov_b32 s4, s56
	global_load_dwordx4 v[240:243], v[70:71], off offset:3072
	global_load_dwordx4 v[236:239], v[72:73], off offset:3072
	global_load_dwordx4 v[232:235], v[74:75], off
	global_load_dwordx4 v[228:231], v[76:77], off
	global_load_dwordx4 v[224:227], v[78:79], off
	global_load_dwordx4 v[220:223], v[80:81], off
	global_load_dwordx4 v[216:219], v[82:83], off
	global_load_dwordx4 v[212:215], v[84:85], off
	global_load_dwordx4 v[208:211], v[86:87], off
	global_load_dwordx4 v[204:207], v[88:89], off
	global_load_dwordx4 v[200:203], v[90:91], off
	global_load_dwordx4 v[196:199], v[92:93], off
	global_load_dwordx4 v[192:195], v[94:95], off
	global_load_dwordx4 v[188:191], v[96:97], off
.LBB0_1510:
	s_ashr_i32 s21, s20, 31
	s_lshl_b64 s[6:7], s[20:21], 2
	v_add_co_u32_e32 v102, vcc, 0xfffff000, v98
	s_add_u32 s8, s14, s6
	v_lshl_add_u64 v[104:105], s[24:25], 0, v[54:55]
	v_addc_co_u32_e32 v103, vcc, -1, v99, vcc
	s_addc_u32 s9, s15, s7
	global_load_dwordx4 v[28:31], v[98:99], off offset:-4096
	global_load_dwordx4 v[24:27], v[98:99], off offset:-3072
	global_load_dwordx4 v[20:23], v[98:99], off offset:-2048
	global_load_dwordx4 v[16:19], v[98:99], off offset:-1024
	global_load_dwordx4 v[12:15], v[98:99], off
	global_load_dwordx4 v[0:3], v[58:59], off
	global_load_dwordx4 v[4:7], v[58:59], off offset:1024
	global_load_dwordx4 v[8:11], v[58:59], off offset:2048
	global_load_dwordx4 v[32:35], v[58:59], off offset:3072
	global_load_dwordx4 v[36:39], v[60:61], off
	global_load_dwordx4 v[40:43], v[62:63], off
	global_load_dwordx4 v[44:47], v[64:65], off
	global_load_dwordx4 v[48:51], v[66:67], off
	global_load_dwordx2 v[118:119], v[104:105], off
	global_load_dwordx2 v[120:121], v[104:105], off offset:512
	global_load_dwordx2 v[122:123], v[104:105], off offset:1024
	global_load_dwordx2 v[124:125], v[104:105], off offset:1536
	global_load_dwordx2 v[126:127], v[104:105], off offset:2048
	global_load_dwordx2 v[128:129], v[104:105], off offset:2560
	global_load_dwordx2 v[130:131], v[104:105], off offset:3072
	global_load_dwordx2 v[132:133], v[104:105], off offset:3584
	global_load_dwordx4 v[110:113], v[102:103], off offset:-3072
	global_load_dwordx4 v[114:117], v[102:103], off offset:-2048
	s_nop 0
	global_load_dwordx4 v[102:105], v[102:103], off offset:-1024
	s_add_u32 s6, s12, s6
	global_load_dwordx2 v[134:135], v53, s[8:9]
	s_addc_u32 s7, s13, s7
	global_load_dwordx2 v[136:137], v53, s[6:7]
	v_lshl_add_u64 v[106:107], s[18:19], 0, v[54:55]
	v_mov_b32_e32 v109, v144
	v_lshl_add_u64 v[100:101], s[16:17], 0, v[54:55]
	s_add_i32 s4, s4, s58
	s_add_i32 s20, s20, s0
	s_add_u32 s24, s24, s26
	s_addc_u32 s25, s25, s27
	s_add_u32 s16, s16, s26
	s_addc_u32 s17, s17, s27
	s_add_u32 s18, s18, s26
	s_addc_u32 s19, s19, s27
	v_lshl_add_u64 v[98:99], v[98:99], 0, s[22:23]
	s_cmpk_lt_i32 s4, 0x2000
	s_waitcnt vmcnt(12)
	v_lshlrev_b32_e32 v138, 16, v118
	v_and_b32_e32 v139, 0xffff0000, v118
	v_lshlrev_b32_e32 v118, 16, v119
	v_and_b32_e32 v119, 0xffff0000, v119
	s_waitcnt vmcnt(11)
	v_lshlrev_b32_e32 v140, 16, v120
	v_and_b32_e32 v141, 0xffff0000, v120
	v_lshlrev_b32_e32 v120, 16, v121
	v_and_b32_e32 v121, 0xffff0000, v121
	s_waitcnt vmcnt(4)
	v_pk_add_f32 v[112:113], v[112:113], v[118:119]
	s_waitcnt vmcnt(3)
	v_pk_add_f32 v[116:117], v[116:117], v[120:121]
	s_waitcnt vmcnt(1)
	v_ashrrev_i32_e32 v119, 31, v134
	v_mov_b32_e32 v118, v134
	v_ashrrev_i32_e32 v121, 31, v135
	v_mov_b32_e32 v120, v135
	v_lshlrev_b64 v[118:119], 12, v[118:119]
	v_lshlrev_b64 v[120:121], 12, v[120:121]
	v_lshlrev_b32_e32 v142, 16, v122
	v_and_b32_e32 v143, 0xffff0000, v122
	v_lshlrev_b32_e32 v122, 16, v123
	v_and_b32_e32 v123, 0xffff0000, v123
	v_lshlrev_b32_e32 v146, 16, v124
	v_and_b32_e32 v147, 0xffff0000, v124
	v_lshlrev_b32_e32 v124, 16, v125
	v_and_b32_e32 v125, 0xffff0000, v125
	v_lshlrev_b32_e32 v148, 16, v126
	v_and_b32_e32 v149, 0xffff0000, v126
	v_lshlrev_b32_e32 v126, 16, v127
	v_and_b32_e32 v127, 0xffff0000, v127
	v_lshlrev_b32_e32 v150, 16, v128
	v_and_b32_e32 v151, 0xffff0000, v128
	v_lshlrev_b32_e32 v128, 16, v129
	v_and_b32_e32 v129, 0xffff0000, v129
	v_lshlrev_b32_e32 v152, 16, v130
	v_and_b32_e32 v153, 0xffff0000, v130
	v_lshlrev_b32_e32 v130, 16, v131
	v_and_b32_e32 v131, 0xffff0000, v131
	v_lshlrev_b32_e32 v154, 16, v132
	v_and_b32_e32 v155, 0xffff0000, v132
	v_lshlrev_b32_e32 v132, 16, v133
	v_and_b32_e32 v133, 0xffff0000, v133
	v_lshl_add_u64 v[118:119], v[56:57], 0, v[118:119]
	v_lshl_add_u64 v[120:121], v[56:57], 0, v[120:121]
	v_pk_add_f32 v[110:111], v[110:111], v[138:139]
	v_pk_add_f32 v[114:115], v[114:115], v[140:141]
	v_pk_add_f32 v[102:103], v[102:103], v[142:143]
	v_pk_add_f32 v[104:105], v[104:105], v[122:123]
	v_pk_add_f32 v[28:29], v[28:29], v[146:147]
	v_pk_add_f32 v[30:31], v[30:31], v[124:125]
	v_pk_add_f32 v[24:25], v[24:25], v[148:149]
	v_pk_add_f32 v[26:27], v[26:27], v[126:127]
	v_pk_add_f32 v[20:21], v[20:21], v[150:151]
	v_pk_add_f32 v[22:23], v[22:23], v[128:129]
	v_pk_add_f32 v[16:17], v[16:17], v[152:153]
	v_pk_add_f32 v[18:19], v[18:19], v[130:131]
	v_pk_add_f32 v[14:15], v[14:15], v[132:133]
	global_load_dwordx2 v[122:123], v[118:119], off
	global_load_dwordx2 v[124:125], v[120:121], off
	global_load_dwordx2 v[126:127], v[118:119], off offset:512
	global_load_dwordx2 v[128:129], v[120:121], off offset:512
	global_load_dwordx2 v[130:131], v[118:119], off offset:1024
	global_load_dwordx2 v[132:133], v[120:121], off offset:1024
	global_load_dwordx2 v[134:135], v[118:119], off offset:1536
	global_load_dwordx2 v[138:139], v[120:121], off offset:1536
	global_load_dwordx2 v[140:141], v[118:119], off offset:2048
	global_load_dwordx2 v[142:143], v[120:121], off offset:2048
	global_load_dwordx2 v[146:147], v[118:119], off offset:2560
	global_load_dwordx2 v[148:149], v[120:121], off offset:2560
	global_load_dwordx2 v[150:151], v[118:119], off offset:3072
	global_load_dwordx2 v[152:153], v[120:121], off offset:3072
	s_nop 0
	global_load_dwordx2 v[118:119], v[118:119], off offset:3584
	s_nop 0
	global_load_dwordx2 v[120:121], v[120:121], off offset:3584
	v_pk_add_f32 v[12:13], v[12:13], v[154:155]
	s_waitcnt vmcnt(15)
	v_lshlrev_b32_e32 v154, 16, v122
	s_waitcnt vmcnt(14)
	v_lshlrev_b32_e32 v156, 16, v124
	v_and_b32_e32 v157, 0xffff0000, v124
	v_lshlrev_b32_e32 v124, 16, v125
	v_and_b32_e32 v125, 0xffff0000, v125
	v_and_b32_e32 v155, 0xffff0000, v122
	v_lshlrev_b32_e32 v122, 16, v123
	v_and_b32_e32 v123, 0xffff0000, v123
	s_waitcnt vmcnt(12)
	v_lshlrev_b32_e32 v160, 16, v128
	v_and_b32_e32 v161, 0xffff0000, v128
	v_lshlrev_b32_e32 v128, 16, v129
	v_and_b32_e32 v129, 0xffff0000, v129
	s_waitcnt vmcnt(10)
	v_lshlrev_b32_e32 v164, 16, v132
	v_and_b32_e32 v165, 0xffff0000, v132
	v_lshlrev_b32_e32 v132, 16, v133
	v_and_b32_e32 v133, 0xffff0000, v133
	s_waitcnt vmcnt(8)
	v_lshlrev_b32_e32 v168, 16, v138
	v_and_b32_e32 v169, 0xffff0000, v138
	v_lshlrev_b32_e32 v138, 16, v139
	v_and_b32_e32 v139, 0xffff0000, v139
	s_waitcnt vmcnt(6)
	v_lshlrev_b32_e32 v172, 16, v142
	v_and_b32_e32 v173, 0xffff0000, v142
	v_lshlrev_b32_e32 v142, 16, v143
	v_and_b32_e32 v143, 0xffff0000, v143
	s_waitcnt vmcnt(4)
	v_lshlrev_b32_e32 v176, 16, v148
	v_and_b32_e32 v177, 0xffff0000, v148
	v_lshlrev_b32_e32 v148, 16, v149
	v_and_b32_e32 v149, 0xffff0000, v149
	s_waitcnt vmcnt(2)
	v_lshlrev_b32_e32 v180, 16, v152
	v_and_b32_e32 v181, 0xffff0000, v152
	v_lshlrev_b32_e32 v152, 16, v153
	v_and_b32_e32 v153, 0xffff0000, v153
	s_waitcnt vmcnt(0)
	v_lshlrev_b32_e32 v184, 16, v120
	v_and_b32_e32 v185, 0xffff0000, v120
	v_lshlrev_b32_e32 v120, 16, v121
	v_and_b32_e32 v121, 0xffff0000, v121
	v_pk_mul_f32 v[156:157], v[136:137], v[156:157] op_sel:[1,0]
	v_pk_mul_f32 v[124:125], v[136:137], v[124:125] op_sel:[1,0]
	v_lshlrev_b32_e32 v158, 16, v126
	v_and_b32_e32 v159, 0xffff0000, v126
	v_lshlrev_b32_e32 v126, 16, v127
	v_and_b32_e32 v127, 0xffff0000, v127
	v_lshlrev_b32_e32 v162, 16, v130
	v_and_b32_e32 v163, 0xffff0000, v130
	v_lshlrev_b32_e32 v130, 16, v131
	v_and_b32_e32 v131, 0xffff0000, v131
	v_lshlrev_b32_e32 v166, 16, v134
	v_and_b32_e32 v167, 0xffff0000, v134
	v_lshlrev_b32_e32 v134, 16, v135
	v_and_b32_e32 v135, 0xffff0000, v135
	v_lshlrev_b32_e32 v170, 16, v140
	v_and_b32_e32 v171, 0xffff0000, v140
	v_lshlrev_b32_e32 v140, 16, v141
	v_and_b32_e32 v141, 0xffff0000, v141
	v_lshlrev_b32_e32 v174, 16, v146
	v_and_b32_e32 v175, 0xffff0000, v146
	v_lshlrev_b32_e32 v146, 16, v147
	v_and_b32_e32 v147, 0xffff0000, v147
	v_lshlrev_b32_e32 v178, 16, v150
	v_and_b32_e32 v179, 0xffff0000, v150
	v_lshlrev_b32_e32 v150, 16, v151
	v_and_b32_e32 v151, 0xffff0000, v151
	v_lshlrev_b32_e32 v182, 16, v118
	v_and_b32_e32 v183, 0xffff0000, v118
	v_lshlrev_b32_e32 v118, 16, v119
	v_and_b32_e32 v119, 0xffff0000, v119
	v_pk_mul_f32 v[160:161], v[136:137], v[160:161] op_sel:[1,0]
	v_pk_mul_f32 v[128:129], v[136:137], v[128:129] op_sel:[1,0]
	v_pk_mul_f32 v[164:165], v[136:137], v[164:165] op_sel:[1,0]
	v_pk_mul_f32 v[132:133], v[136:137], v[132:133] op_sel:[1,0]
	v_pk_mul_f32 v[168:169], v[136:137], v[168:169] op_sel:[1,0]
	v_pk_mul_f32 v[138:139], v[136:137], v[138:139] op_sel:[1,0]
	v_pk_mul_f32 v[172:173], v[136:137], v[172:173] op_sel:[1,0]
	v_pk_mul_f32 v[142:143], v[136:137], v[142:143] op_sel:[1,0]
	v_pk_mul_f32 v[176:177], v[136:137], v[176:177] op_sel:[1,0]
	v_pk_mul_f32 v[148:149], v[136:137], v[148:149] op_sel:[1,0]
	v_pk_mul_f32 v[180:181], v[136:137], v[180:181] op_sel:[1,0]
	v_pk_mul_f32 v[152:153], v[136:137], v[152:153] op_sel:[1,0]
	v_pk_mul_f32 v[184:185], v[136:137], v[184:185] op_sel:[1,0]
	v_pk_mul_f32 v[120:121], v[136:137], v[120:121] op_sel:[1,0]
	v_pk_fma_f32 v[154:155], v[136:137], v[154:155], v[156:157] op_sel_hi:[0,1,1]
	v_pk_fma_f32 v[122:123], v[136:137], v[122:123], v[124:125] op_sel_hi:[0,1,1]
	v_pk_fma_f32 v[124:125], v[136:137], v[158:159], v[160:161] op_sel_hi:[0,1,1]
	v_pk_fma_f32 v[126:127], v[136:137], v[126:127], v[128:129] op_sel_hi:[0,1,1]
	v_pk_fma_f32 v[128:129], v[136:137], v[162:163], v[164:165] op_sel_hi:[0,1,1]
	v_pk_fma_f32 v[130:131], v[136:137], v[130:131], v[132:133] op_sel_hi:[0,1,1]
	v_pk_fma_f32 v[132:133], v[136:137], v[166:167], v[168:169] op_sel_hi:[0,1,1]
	v_pk_fma_f32 v[134:135], v[136:137], v[134:135], v[138:139] op_sel_hi:[0,1,1]
	v_pk_fma_f32 v[138:139], v[136:137], v[170:171], v[172:173] op_sel_hi:[0,1,1]
	v_pk_fma_f32 v[140:141], v[136:137], v[140:141], v[142:143] op_sel_hi:[0,1,1]
	v_pk_fma_f32 v[142:143], v[136:137], v[174:175], v[176:177] op_sel_hi:[0,1,1]
	v_pk_fma_f32 v[146:147], v[136:137], v[146:147], v[148:149] op_sel_hi:[0,1,1]
	v_pk_fma_f32 v[148:149], v[136:137], v[178:179], v[180:181] op_sel_hi:[0,1,1]
	v_pk_fma_f32 v[150:151], v[136:137], v[150:151], v[152:153] op_sel_hi:[0,1,1]
	v_pk_fma_f32 v[152:153], v[136:137], v[182:183], v[184:185] op_sel_hi:[0,1,1]
	v_pk_fma_f32 v[118:119], v[136:137], v[118:119], v[120:121] op_sel_hi:[0,1,1]
	v_pk_fma_f32 v[0:1], v[0:1], v[154:155], v[110:111]
	v_pk_fma_f32 v[2:3], v[2:3], v[122:123], v[112:113]
	v_pk_fma_f32 v[4:5], v[4:5], v[124:125], v[114:115]
	v_pk_fma_f32 v[6:7], v[6:7], v[126:127], v[116:117]
	v_pk_fma_f32 v[8:9], v[8:9], v[128:129], v[102:103]
	v_pk_fma_f32 v[10:11], v[10:11], v[130:131], v[104:105]
	v_pk_fma_f32 v[28:29], v[32:33], v[132:133], v[28:29]
	v_pk_fma_f32 v[30:31], v[34:35], v[134:135], v[30:31]
	v_pk_fma_f32 v[24:25], v[36:37], v[138:139], v[24:25]
	v_pk_fma_f32 v[26:27], v[38:39], v[140:141], v[26:27]
	v_pk_fma_f32 v[20:21], v[40:41], v[142:143], v[20:21]
	v_pk_fma_f32 v[22:23], v[42:43], v[146:147], v[22:23]
	v_pk_fma_f32 v[16:17], v[44:45], v[148:149], v[16:17]
	v_pk_fma_f32 v[18:19], v[46:47], v[150:151], v[18:19]
	v_pk_fma_f32 v[12:13], v[48:49], v[152:153], v[12:13]
	v_pk_fma_f32 v[14:15], v[50:51], v[118:119], v[14:15]
	v_cvt_pk_bf16_f32 v0, v0, v1
	v_cvt_pk_bf16_f32 v1, v2, v3
	v_cvt_pk_bf16_f32 v2, v4, v5
	v_cvt_pk_bf16_f32 v3, v6, v7
	v_cvt_pk_bf16_f32 v4, v8, v9
	v_cvt_pk_bf16_f32 v5, v10, v11
	v_cvt_pk_bf16_f32 v28, v28, v29
	v_cvt_pk_bf16_f32 v29, v30, v31
	v_cvt_pk_bf16_f32 v24, v24, v25
	v_cvt_pk_bf16_f32 v25, v26, v27
	v_cvt_pk_bf16_f32 v20, v20, v21
	v_cvt_pk_bf16_f32 v21, v22, v23
	v_cvt_pk_bf16_f32 v22, v16, v17
	v_cvt_pk_bf16_f32 v23, v18, v19
	v_cvt_pk_bf16_f32 v18, v12, v13
	v_cvt_pk_bf16_f32 v19, v14, v15
	global_store_dwordx2 v[106:107], v[0:1], off
	global_store_dwordx2 v[106:107], v[2:3], off offset:512
	global_store_dwordx2 v[106:107], v[4:5], off offset:1024
	global_store_dwordx2 v[106:107], v[28:29], off offset:1536
	global_store_dwordx2 v[106:107], v[24:25], off offset:2048
	global_store_dwordx2 v[106:107], v[20:21], off offset:2560
	global_store_dwordx2 v[106:107], v[22:23], off offset:3072
	global_store_dwordx2 v[106:107], v[18:19], off offset:3584
	global_load_dwordx4 v[6:9], v[68:69], off
	global_load_dwordx4 v[10:13], v[70:71], off
	global_load_dwordx4 v[14:17], v[72:73], off
	v_and_b32_e32 v27, 0xffff0000, v1
	v_and_b32_e32 v31, 0xffff0000, v0
	v_and_b32_e32 v33, 0xffff0000, v3
	v_and_b32_e32 v35, 0xffff0000, v2
	v_lshlrev_b32_e32 v26, 16, v1
	v_lshlrev_b32_e32 v30, 16, v0
	v_lshlrev_b32_e32 v32, 16, v3
	v_lshlrev_b32_e32 v34, 16, v2
	v_lshlrev_b32_e32 v36, 16, v5
	v_and_b32_e32 v37, 0xffff0000, v5
	v_lshlrev_b32_e32 v38, 16, v4
	v_and_b32_e32 v39, 0xffff0000, v4
	v_lshlrev_b32_e32 v40, 16, v29
	v_and_b32_e32 v41, 0xffff0000, v29
	v_lshlrev_b32_e32 v42, 16, v28
	v_and_b32_e32 v43, 0xffff0000, v28
	v_lshlrev_b32_e32 v28, 16, v25
	v_and_b32_e32 v29, 0xffff0000, v25
	v_lshlrev_b32_e32 v44, 16, v24
	v_and_b32_e32 v45, 0xffff0000, v24
	v_lshlrev_b32_e32 v24, 16, v21
	v_and_b32_e32 v25, 0xffff0000, v21
	v_lshlrev_b32_e32 v46, 16, v20
	v_and_b32_e32 v47, 0xffff0000, v20
	v_lshlrev_b32_e32 v4, 16, v23
	v_and_b32_e32 v5, 0xffff0000, v23
	v_lshlrev_b32_e32 v20, 16, v22
	v_and_b32_e32 v21, 0xffff0000, v22
	v_mov_b32_e32 v22, v27
	v_mov_b32_e32 v23, v33
	v_mov_b32_e32 v50, v31
	v_mov_b32_e32 v51, v35
	v_lshlrev_b32_e32 v0, 16, v19
	v_and_b32_e32 v1, 0xffff0000, v19
	v_lshlrev_b32_e32 v2, 16, v18
	v_and_b32_e32 v3, 0xffff0000, v18
	v_mov_b32_e32 v18, v26
	v_mov_b32_e32 v19, v32
	v_mov_b32_e32 v48, v30
	v_mov_b32_e32 v49, v34
	v_mov_b32_e32 v104, v39
	v_mov_b32_e32 v105, v37
	v_pk_mul_f32 v[22:23], v[22:23], v[22:23]
	v_pk_mul_f32 v[50:51], v[50:51], v[50:51]
	v_mov_b32_e32 v102, v38
	v_mov_b32_e32 v103, v36
	v_pk_mul_f32 v[104:105], v[104:105], v[104:105]
	v_pk_fma_f32 v[18:19], v[18:19], v[18:19], v[22:23]
	v_pk_fma_f32 v[22:23], v[48:49], v[48:49], v[50:51]
	v_lshlrev_b32_e32 v107, 2, v109
	v_mul_f32_e32 v106, v41, v41
	v_mul_f32_e32 v110, v43, v43
	v_pk_fma_f32 v[48:49], v[102:103], v[102:103], v[104:105]
	v_pk_add_f32 v[18:19], v[22:23], v[18:19]
	v_pk_mul_f32 v[112:113], v[28:29], v[28:29]
	v_pk_mul_f32 v[114:115], v[44:45], v[44:45]
	v_xor_b32_e32 v109, 4, v107
	v_xor_b32_e32 v128, 8, v107
	v_xor_b32_e32 v129, 16, v107
	v_xor_b32_e32 v130, 32, v107
	v_xor_b32_e32 v131, 64, v107
	v_xor_b32_e32 v132, 0x80, v107
	v_pk_fma_f32 v[106:107], v[40:41], v[40:41], v[106:107] op_sel_hi:[1,1,0]
	v_pk_fma_f32 v[110:111], v[42:43], v[42:43], v[110:111] op_sel_hi:[1,1,0]
	v_pk_add_f32 v[22:23], v[48:49], v[48:49] op_sel:[0,1] op_sel_hi:[1,0]
	v_pk_add_f32 v[18:19], v[18:19], v[18:19] op_sel:[0,1] op_sel_hi:[1,0]
	v_mov_b32_e32 v118, v47
	v_mov_b32_e32 v119, v25
	v_mov_b32_e32 v111, v112
	v_mov_b32_e32 v107, v113
	v_mov_b32_e32 v23, v115
	v_mov_b32_e32 v19, v114
	v_mov_b32_e32 v116, v46
	v_mov_b32_e32 v117, v24
	v_pk_mul_f32 v[118:119], v[118:119], v[118:119]
	v_pk_add_f32 v[48:49], v[110:111], v[106:107]
	v_pk_add_f32 v[18:19], v[18:19], v[22:23]
	v_mul_f32_e32 v120, v5, v5
	v_mul_f32_e32 v122, v21, v21
	v_pk_fma_f32 v[50:51], v[116:117], v[116:117], v[118:119]
	v_pk_add_f32 v[18:19], v[18:19], v[48:49]
	v_pk_mul_f32 v[124:125], v[0:1], v[0:1]
	v_pk_mul_f32 v[126:127], v[2:3], v[2:3]
	v_pk_fma_f32 v[120:121], v[4:5], v[4:5], v[120:121] op_sel_hi:[1,1,0]
	v_pk_fma_f32 v[122:123], v[20:21], v[20:21], v[122:123] op_sel_hi:[1,1,0]
	v_pk_add_f32 v[50:51], v[50:51], v[50:51] op_sel:[0,1] op_sel_hi:[1,0]
	v_pk_add_f32 v[18:19], v[18:19], v[18:19] op_sel:[0,1] op_sel_hi:[1,0]
	v_mov_b32_e32 v123, v124
	v_mov_b32_e32 v121, v125
	v_mov_b32_e32 v51, v127
	v_mov_b32_e32 v19, v126
	v_pk_add_f32 v[102:103], v[122:123], v[120:121]
	v_pk_add_f32 v[18:19], v[18:19], v[50:51]
	s_waitcnt vmcnt(1)
	v_pk_add_f32 v[10:11], v[10:11], 1.0 op_sel_hi:[1,0]
	v_pk_add_f32 v[18:19], v[18:19], v[102:103]
	v_pk_add_f32 v[12:13], v[12:13], 1.0 op_sel_hi:[1,0]
	v_add_f32_e32 v18, v18, v19
	ds_bpermute_b32 v19, v109, v18
	s_waitcnt lgkmcnt(0)
	v_add_f32_e32 v18, v18, v19
	ds_bpermute_b32 v19, v128, v18
	s_waitcnt lgkmcnt(0)
	v_add_f32_e32 v18, v18, v19
	ds_bpermute_b32 v19, v129, v18
	s_waitcnt lgkmcnt(0)
	v_add_f32_e32 v18, v18, v19
	ds_bpermute_b32 v19, v130, v18
	s_waitcnt lgkmcnt(0)
	v_add_f32_e32 v18, v18, v19
	ds_bpermute_b32 v19, v131, v18
	s_waitcnt lgkmcnt(0)
	v_add_f32_e32 v18, v18, v19
	ds_bpermute_b32 v19, v132, v18
	s_waitcnt lgkmcnt(0)
	v_add_f32_e32 v18, v18, v19
	v_fmamk_f32 v18, v18, 0x3a000000, v108
	v_mul_f32_e32 v19, 0x4b800000, v18
	v_cmp_gt_f32_e32 vcc, s1, v18
	s_nop 1
	v_cndmask_b32_e32 v18, v18, v19, vcc
	v_rsq_f32_e32 v18, v18
	s_nop 0
	v_mul_f32_e32 v19, 0x45800000, v18
	v_cndmask_b32_e32 v18, v18, v19, vcc
	v_pk_mul_f32 v[22:23], v[18:19], v[30:31] op_sel_hi:[0,1]
	v_pk_mul_f32 v[26:27], v[18:19], v[26:27] op_sel_hi:[0,1]
	v_pk_mul_f32 v[6:7], v[6:7], v[22:23]
	v_pk_mul_f32 v[8:9], v[8:9], v[26:27]
	s_waitcnt vmcnt(0)
	v_pk_fma_f32 v[6:7], v[10:11], v[6:7], v[14:15]
	v_pk_fma_f32 v[8:9], v[12:13], v[8:9], v[16:17]
	v_cvt_pk_bf16_f32 v6, v6, v7
	v_cvt_pk_bf16_f32 v7, v8, v9
	global_store_dwordx2 v[100:101], v[6:7], off
	global_load_dwordx4 v[6:9], v[68:69], off offset:1024
	s_nop 0
	global_load_dwordx4 v[10:13], v[70:71], off offset:1024
	global_load_dwordx4 v[14:17], v[72:73], off offset:1024
	v_pk_mul_f32 v[22:23], v[18:19], v[34:35] op_sel_hi:[0,1]
	v_pk_mul_f32 v[26:27], v[18:19], v[32:33] op_sel_hi:[0,1]
	v_pk_mul_f32 v[24:25], v[18:19], v[24:25] op_sel_hi:[0,1]
	v_pk_mul_f32 v[20:21], v[18:19], v[20:21] op_sel_hi:[0,1]
	v_pk_mul_f32 v[4:5], v[18:19], v[4:5] op_sel_hi:[0,1]
	v_pk_mul_f32 v[2:3], v[18:19], v[2:3] op_sel_hi:[0,1]
	v_pk_mul_f32 v[0:1], v[18:19], v[0:1] op_sel_hi:[0,1]
	s_waitcnt vmcnt(2)
	v_pk_mul_f32 v[6:7], v[6:7], v[22:23]
	s_waitcnt vmcnt(1)
	v_pk_add_f32 v[10:11], v[10:11], 1.0 op_sel_hi:[1,0]
	v_pk_mul_f32 v[8:9], v[8:9], v[26:27]
	v_pk_add_f32 v[12:13], v[12:13], 1.0 op_sel_hi:[1,0]
	s_waitcnt vmcnt(0)
	v_pk_fma_f32 v[6:7], v[10:11], v[6:7], v[14:15]
	v_pk_fma_f32 v[8:9], v[12:13], v[8:9], v[16:17]
	v_cvt_pk_bf16_f32 v6, v6, v7
	v_cvt_pk_bf16_f32 v7, v8, v9
	global_store_dwordx2 v[100:101], v[6:7], off offset:512
	global_load_dwordx4 v[6:9], v[68:69], off offset:2048
	s_nop 0
	global_load_dwordx4 v[10:13], v[70:71], off offset:2048
	global_load_dwordx4 v[14:17], v[72:73], off offset:2048
	v_pk_mul_f32 v[22:23], v[18:19], v[38:39] op_sel_hi:[0,1]
	v_pk_mul_f32 v[26:27], v[18:19], v[36:37] op_sel_hi:[0,1]
	s_waitcnt vmcnt(2)
	v_pk_mul_f32 v[6:7], v[6:7], v[22:23]
	s_waitcnt vmcnt(1)
	v_pk_add_f32 v[10:11], v[10:11], 1.0 op_sel_hi:[1,0]
	v_pk_mul_f32 v[8:9], v[8:9], v[26:27]
	v_pk_add_f32 v[12:13], v[12:13], 1.0 op_sel_hi:[1,0]
	s_waitcnt vmcnt(0)
	v_pk_fma_f32 v[6:7], v[10:11], v[6:7], v[14:15]
	v_pk_fma_f32 v[8:9], v[12:13], v[8:9], v[16:17]
	v_cvt_pk_bf16_f32 v6, v6, v7
	v_cvt_pk_bf16_f32 v7, v8, v9
	global_store_dwordx2 v[100:101], v[6:7], off offset:1024
	global_load_dwordx4 v[6:9], v[68:69], off offset:3072
	s_nop 0
	v_pk_mul_f32 v[22:23], v[18:19], v[42:43] op_sel_hi:[0,1]
	v_pk_mul_f32 v[26:27], v[18:19], v[40:41] op_sel_hi:[0,1]
	s_waitcnt vmcnt(0)
	v_pk_mul_f32 v[6:7], v[6:7], v[22:23]
	v_pk_add_f32 v[10:11], v[240:241], 1.0 op_sel_hi:[1,0]
	v_pk_mul_f32 v[8:9], v[8:9], v[26:27]
	v_pk_add_f32 v[12:13], v[242:243], 1.0 op_sel_hi:[1,0]
	v_pk_fma_f32 v[6:7], v[10:11], v[6:7], v[236:237]
	v_pk_fma_f32 v[8:9], v[12:13], v[8:9], v[238:239]
	v_cvt_pk_bf16_f32 v6, v6, v7
	v_cvt_pk_bf16_f32 v7, v8, v9
	global_store_dwordx2 v[100:101], v[6:7], off offset:1536
	s_nop 0
	v_pk_mul_f32 v[22:23], v[18:19], v[44:45] op_sel_hi:[0,1]
	v_pk_mul_f32 v[26:27], v[18:19], v[28:29] op_sel_hi:[0,1]
	v_pk_mul_f32 v[6:7], v[22:23], v[232:233]
	v_pk_add_f32 v[10:11], v[228:229], 1.0 op_sel_hi:[1,0]
	v_pk_mul_f32 v[8:9], v[26:27], v[234:235]
	v_pk_add_f32 v[12:13], v[230:231], 1.0 op_sel_hi:[1,0]
	v_pk_fma_f32 v[6:7], v[6:7], v[10:11], v[224:225]
	v_pk_fma_f32 v[8:9], v[8:9], v[12:13], v[226:227]
	v_cvt_pk_bf16_f32 v6, v6, v7
	v_cvt_pk_bf16_f32 v7, v8, v9
	global_store_dwordx2 v[100:101], v[6:7], off offset:2048
	s_nop 0
	v_pk_mul_f32 v[22:23], v[18:19], v[46:47] op_sel_hi:[0,1]
	v_pk_mul_f32 v[6:7], v[22:23], v[220:221]
	v_pk_add_f32 v[10:11], v[216:217], 1.0 op_sel_hi:[1,0]
	v_pk_mul_f32 v[8:9], v[24:25], v[222:223]
	v_pk_add_f32 v[12:13], v[218:219], 1.0 op_sel_hi:[1,0]
	v_pk_fma_f32 v[6:7], v[6:7], v[10:11], v[212:213]
	v_pk_fma_f32 v[8:9], v[8:9], v[12:13], v[214:215]
	v_cvt_pk_bf16_f32 v6, v6, v7
	v_cvt_pk_bf16_f32 v7, v8, v9
	global_store_dwordx2 v[100:101], v[6:7], off offset:2560
	s_nop 0
	v_pk_mul_f32 v[6:7], v[20:21], v[208:209]
	v_pk_add_f32 v[10:11], v[204:205], 1.0 op_sel_hi:[1,0]
	v_pk_mul_f32 v[4:5], v[4:5], v[210:211]
	v_pk_add_f32 v[8:9], v[206:207], 1.0 op_sel_hi:[1,0]
	v_pk_fma_f32 v[6:7], v[6:7], v[10:11], v[200:201]
	v_pk_fma_f32 v[4:5], v[4:5], v[8:9], v[202:203]
	v_cvt_pk_bf16_f32 v6, v6, v7
	v_cvt_pk_bf16_f32 v7, v4, v5
	global_store_dwordx2 v[100:101], v[6:7], off offset:3072
	s_nop 0
	v_pk_mul_f32 v[2:3], v[2:3], v[196:197]
	v_pk_add_f32 v[4:5], v[192:193], 1.0 op_sel_hi:[1,0]
	v_pk_mul_f32 v[0:1], v[0:1], v[198:199]
	v_pk_add_f32 v[6:7], v[194:195], 1.0 op_sel_hi:[1,0]
	v_pk_fma_f32 v[2:3], v[2:3], v[4:5], v[188:189]
	v_pk_fma_f32 v[0:1], v[0:1], v[6:7], v[190:191]
	v_cvt_pk_bf16_f32 v2, v2, v3
	v_cvt_pk_bf16_f32 v3, v0, v1
	global_store_dwordx2 v[100:101], v[2:3], off offset:3584
	s_cbranch_scc1 .LBB0_1510

.LBB0_2855:
	s_or_b64 exec, exec, s[36:37]
	v_readlane_b32 s0, v247, 25
	v_readlane_b32 s1, v247, 26
	v_readlane_b32 s14, v247, 9
	s_and_b64 vcc, exec, s[0:1]
	v_readlane_b32 s15, v247, 10
	s_waitcnt lgkmcnt(0)
	s_barrier
	s_cbranch_vccnz .LBB0_2858
	s_load_dwordx4 s[4:7], s[14:15], 0x190
	s_load_dwordx2 s[0:1], s[14:15], 0x1c8
	s_load_dwordx2 s[12:13], s[14:15], 0x130
	s_load_dwordx2 s[8:9], s[14:15], 0xc8
	s_load_dwordx2 s[10:11], s[14:15], 0xd8
	s_load_dwordx2 s[16:17], s[14:15], 0x120
	v_ashrrev_i32_e32 v145, 31, v144
	v_lshlrev_b64 v[32:33], 3, v[144:145]
	v_lshlrev_b64 v[0:1], 4, v[144:145]
	s_waitcnt lgkmcnt(0)
	v_lshl_add_u64 v[34:35], s[0:1], 0, v[32:33]
	v_lshl_add_u64 v[2:3], s[10:11], 0, v[0:1]
	s_mov_b64 s[0:1], 0x16000
	v_lshl_add_u64 v[36:37], v[2:3], 0, s[0:1]
	s_mov_b64 s[0:1], 0x17000
	v_lshl_add_u64 v[38:39], v[2:3], 0, s[0:1]
	s_mov_b64 s[0:1], 0x17400
	v_lshl_add_u64 v[40:41], v[2:3], 0, s[0:1]
	s_mov_b64 s[0:1], 0x17800
	v_lshl_add_u64 v[42:43], v[2:3], 0, s[0:1]
	s_mov_b64 s[0:1], 0x17c00
	v_lshl_add_u64 v[44:45], v[2:3], 0, s[0:1]
	s_lshl_b32 s0, s2, 4
	s_lshl_b32 s1, s33, 1
	s_ashr_i32 s57, s56, 31
	s_add_i32 s0, s0, s1
	s_lshl_b32 s14, s3, 4
	s_lshl_b64 s[2:3], s[56:57], 13
	s_add_u32 s2, s8, s2
	s_addc_u32 s3, s9, s3
	v_lshl_add_u64 v[0:1], s[2:3], 0, v[0:1]
	s_mov_b64 s[2:3], 0x1c00
	s_ashr_i32 s59, s58, 31
	v_lshl_add_u64 v[46:47], v[0:1], 0, s[2:3]
	s_lshl_b64 s[2:3], s[58:59], 13
	s_lshl_b64 s[18:19], s[56:57], 12
	s_add_u32 s8, s16, s18
	s_addc_u32 s9, s17, s19
	s_lshl_b64 s[10:11], s[58:59], 12
	s_add_u32 s12, s12, s18
	s_addc_u32 s13, s13, s19
	v_mov_b32_e32 v54, 0
	s_movk_i32 s15, 0xf000
	global_load_dwordx4 v[180:183], v[36:37], off
	global_load_dwordx4 v[176:179], v[36:37], off offset:1024
	global_load_dwordx4 v[172:175], v[36:37], off offset:2048
	global_load_dwordx4 v[168:171], v[36:37], off offset:3072
	global_load_dwordx4 v[164:167], v[38:39], off
	global_load_dwordx4 v[160:163], v[40:41], off
	global_load_dwordx4 v[156:159], v[42:43], off
	global_load_dwordx4 v[152:155], v[44:45], off
.LBB0_2857:
	s_ashr_i32 s1, s0, 31
	s_lshl_b64 s[16:17], s[0:1], 2
	v_lshl_add_u64 v[48:49], s[8:9], 0, v[32:33]
	s_add_u32 s18, s6, s16
	v_lshl_add_u64 v[50:51], s[12:13], 0, v[32:33]
	global_load_dwordx2 v[56:57], v[48:49], off
	global_load_dwordx2 v[58:59], v[50:51], off
	global_load_dwordx2 v[60:61], v[48:49], off offset:512
	global_load_dwordx2 v[62:63], v[50:51], off offset:512
	global_load_dwordx2 v[64:65], v[48:49], off offset:1024
	global_load_dwordx2 v[66:67], v[50:51], off offset:1024
	global_load_dwordx2 v[68:69], v[48:49], off offset:1536
	global_load_dwordx2 v[70:71], v[50:51], off offset:1536
	global_load_dwordx2 v[72:73], v[48:49], off offset:2048
	global_load_dwordx2 v[74:75], v[50:51], off offset:2048
	global_load_dwordx2 v[76:77], v[48:49], off offset:2560
	global_load_dwordx2 v[78:79], v[50:51], off offset:2560
	global_load_dwordx2 v[80:81], v[48:49], off offset:3072
	global_load_dwordx2 v[82:83], v[50:51], off offset:3072
	global_load_dwordx2 v[84:85], v[48:49], off offset:3584
	s_nop 0
	global_load_dwordx2 v[48:49], v[50:51], off offset:3584
	s_addc_u32 s19, s7, s17
	global_load_dwordx2 v[50:51], v54, s[18:19]
	s_add_u32 s16, s4, s16
	s_addc_u32 s17, s5, s17
	global_load_dwordx2 v[86:87], v54, s[16:17]
	s_add_i32 s56, s56, s58
	s_add_i32 s0, s0, s14
	s_add_u32 s8, s8, s10
	s_addc_u32 s9, s9, s11
	v_add_co_u32_e32 v52, vcc, s15, v46
	s_add_u32 s12, s12, s10
	s_nop 0
	v_addc_co_u32_e32 v53, vcc, -1, v47, vcc
	s_addc_u32 s13, s13, s11
	s_cmpk_lt_i32 s56, 0x2000
	s_waitcnt vmcnt(17)
	v_lshlrev_b32_e32 v88, 16, v56
	v_and_b32_e32 v89, 0xffff0000, v56
	s_waitcnt vmcnt(16)
	v_lshlrev_b32_e32 v90, 16, v58
	v_and_b32_e32 v91, 0xffff0000, v58
	v_pk_add_f32 v[88:89], v[88:89], v[90:91]
	v_lshlrev_b32_e32 v56, 16, v57
	v_and_b32_e32 v57, 0xffff0000, v57
	v_lshlrev_b32_e32 v58, 16, v59
	v_and_b32_e32 v59, 0xffff0000, v59
	s_waitcnt vmcnt(15)
	v_lshlrev_b32_e32 v92, 16, v60
	v_and_b32_e32 v93, 0xffff0000, v60
	s_waitcnt vmcnt(14)
	v_lshlrev_b32_e32 v94, 16, v62
	v_and_b32_e32 v95, 0xffff0000, v62
	v_lshlrev_b32_e32 v60, 16, v61
	s_waitcnt vmcnt(3)
	v_lshlrev_b32_e32 v116, 16, v84
	v_and_b32_e32 v117, 0xffff0000, v84
	s_waitcnt vmcnt(2)
	v_lshlrev_b32_e32 v118, 16, v48
	v_and_b32_e32 v119, 0xffff0000, v48
	v_lshlrev_b32_e32 v84, 16, v85
	v_and_b32_e32 v85, 0xffff0000, v85
	v_lshlrev_b32_e32 v48, 16, v49
	v_and_b32_e32 v49, 0xffff0000, v49
	v_pk_add_f32 v[48:49], v[84:85], v[48:49]
	s_waitcnt vmcnt(1)
	v_ashrrev_i32_e32 v85, 31, v50
	v_mov_b32_e32 v84, v50
	v_ashrrev_i32_e32 v91, 31, v51
	v_mov_b32_e32 v90, v51
	v_lshlrev_b64 v[50:51], 12, v[84:85]
	v_and_b32_e32 v61, 0xffff0000, v61
	v_lshlrev_b32_e32 v62, 16, v63
	v_and_b32_e32 v63, 0xffff0000, v63
	v_lshlrev_b32_e32 v96, 16, v64
	v_and_b32_e32 v97, 0xffff0000, v64
	v_lshlrev_b32_e32 v98, 16, v66
	v_and_b32_e32 v99, 0xffff0000, v66
	v_lshlrev_b32_e32 v64, 16, v65
	v_and_b32_e32 v65, 0xffff0000, v65
	v_lshlrev_b32_e32 v66, 16, v67
	v_and_b32_e32 v67, 0xffff0000, v67
	v_lshlrev_b32_e32 v100, 16, v68
	v_and_b32_e32 v101, 0xffff0000, v68
	v_lshlrev_b32_e32 v102, 16, v70
	v_and_b32_e32 v103, 0xffff0000, v70
	v_lshlrev_b32_e32 v68, 16, v69
	v_and_b32_e32 v69, 0xffff0000, v69
	v_lshlrev_b32_e32 v70, 16, v71
	v_and_b32_e32 v71, 0xffff0000, v71
	v_lshlrev_b32_e32 v104, 16, v72
	v_and_b32_e32 v105, 0xffff0000, v72
	v_lshlrev_b32_e32 v106, 16, v74
	v_and_b32_e32 v107, 0xffff0000, v74
	v_lshlrev_b32_e32 v72, 16, v73
	v_and_b32_e32 v73, 0xffff0000, v73
	v_lshlrev_b32_e32 v74, 16, v75
	v_and_b32_e32 v75, 0xffff0000, v75
	v_lshlrev_b32_e32 v108, 16, v76
	v_and_b32_e32 v109, 0xffff0000, v76
	v_lshlrev_b32_e32 v110, 16, v78
	v_and_b32_e32 v111, 0xffff0000, v78
	v_lshlrev_b32_e32 v76, 16, v77
	v_and_b32_e32 v77, 0xffff0000, v77
	v_lshlrev_b32_e32 v78, 16, v79
	v_and_b32_e32 v79, 0xffff0000, v79
	v_lshlrev_b32_e32 v112, 16, v80
	v_and_b32_e32 v113, 0xffff0000, v80
	v_lshlrev_b32_e32 v114, 16, v82
	v_and_b32_e32 v115, 0xffff0000, v82
	v_lshlrev_b32_e32 v80, 16, v81
	v_and_b32_e32 v81, 0xffff0000, v81
	v_lshlrev_b32_e32 v82, 16, v83
	v_and_b32_e32 v83, 0xffff0000, v83
	v_lshlrev_b64 v[84:85], 12, v[90:91]
	v_lshl_add_u64 v[50:51], v[34:35], 0, v[50:51]
	v_pk_add_f32 v[56:57], v[56:57], v[58:59]
	v_pk_add_f32 v[58:59], v[92:93], v[94:95]
	v_pk_add_f32 v[60:61], v[60:61], v[62:63]
	v_pk_add_f32 v[62:63], v[96:97], v[98:99]
	v_pk_add_f32 v[64:65], v[64:65], v[66:67]
	v_pk_add_f32 v[66:67], v[100:101], v[102:103]
	v_pk_add_f32 v[68:69], v[68:69], v[70:71]
	v_pk_add_f32 v[70:71], v[104:105], v[106:107]
	v_pk_add_f32 v[72:73], v[72:73], v[74:75]
	v_pk_add_f32 v[74:75], v[108:109], v[110:111]
	v_pk_add_f32 v[76:77], v[76:77], v[78:79]
	v_pk_add_f32 v[78:79], v[112:113], v[114:115]
	v_pk_add_f32 v[80:81], v[80:81], v[82:83]
	v_pk_add_f32 v[82:83], v[116:117], v[118:119]
	v_lshl_add_u64 v[84:85], v[34:35], 0, v[84:85]
	global_load_dwordx2 v[90:91], v[50:51], off
	global_load_dwordx2 v[92:93], v[84:85], off
	global_load_dwordx2 v[94:95], v[50:51], off offset:512
	global_load_dwordx2 v[96:97], v[84:85], off offset:512
	global_load_dwordx2 v[98:99], v[50:51], off offset:1024
	global_load_dwordx2 v[100:101], v[84:85], off offset:1024
	global_load_dwordx2 v[102:103], v[50:51], off offset:1536
	global_load_dwordx2 v[104:105], v[84:85], off offset:1536
	global_load_dwordx2 v[106:107], v[50:51], off offset:2048
	global_load_dwordx2 v[108:109], v[84:85], off offset:2048
	global_load_dwordx2 v[110:111], v[50:51], off offset:2560
	global_load_dwordx2 v[112:113], v[84:85], off offset:2560
	global_load_dwordx2 v[114:115], v[50:51], off offset:3072
	global_load_dwordx2 v[116:117], v[84:85], off offset:3072
	global_load_dwordx2 v[118:119], v[50:51], off offset:3584
	s_nop 0
	global_load_dwordx2 v[50:51], v[84:85], off offset:3584
	s_waitcnt vmcnt(15)
	v_lshlrev_b32_e32 v84, 16, v90
	s_waitcnt vmcnt(14)
	v_lshlrev_b32_e32 v120, 16, v92
	v_and_b32_e32 v121, 0xffff0000, v92
	v_lshlrev_b32_e32 v92, 16, v93
	v_and_b32_e32 v93, 0xffff0000, v93
	v_and_b32_e32 v85, 0xffff0000, v90
	v_lshlrev_b32_e32 v90, 16, v91
	v_and_b32_e32 v91, 0xffff0000, v91
	s_waitcnt vmcnt(12)
	v_lshlrev_b32_e32 v124, 16, v96
	v_and_b32_e32 v125, 0xffff0000, v96
	v_lshlrev_b32_e32 v96, 16, v97
	v_and_b32_e32 v97, 0xffff0000, v97
	s_waitcnt vmcnt(10)
	v_lshlrev_b32_e32 v128, 16, v100
	v_and_b32_e32 v129, 0xffff0000, v100
	v_lshlrev_b32_e32 v100, 16, v101
	v_and_b32_e32 v101, 0xffff0000, v101
	s_waitcnt vmcnt(8)
	v_lshlrev_b32_e32 v132, 16, v104
	v_and_b32_e32 v133, 0xffff0000, v104
	v_lshlrev_b32_e32 v104, 16, v105
	v_and_b32_e32 v105, 0xffff0000, v105
	s_waitcnt vmcnt(6)
	v_lshlrev_b32_e32 v136, 16, v108
	v_and_b32_e32 v137, 0xffff0000, v108
	v_lshlrev_b32_e32 v108, 16, v109
	v_and_b32_e32 v109, 0xffff0000, v109
	s_waitcnt vmcnt(4)
	v_lshlrev_b32_e32 v140, 16, v112
	v_and_b32_e32 v141, 0xffff0000, v112
	v_lshlrev_b32_e32 v112, 16, v113
	v_and_b32_e32 v113, 0xffff0000, v113
	s_waitcnt vmcnt(2)
	v_lshlrev_b32_e32 v144, 16, v116
	v_and_b32_e32 v145, 0xffff0000, v116
	v_lshlrev_b32_e32 v116, 16, v117
	v_and_b32_e32 v117, 0xffff0000, v117
	s_waitcnt vmcnt(0)
	v_lshlrev_b32_e32 v148, 16, v50
	v_and_b32_e32 v149, 0xffff0000, v50
	v_lshlrev_b32_e32 v50, 16, v51
	v_and_b32_e32 v51, 0xffff0000, v51
	v_pk_mul_f32 v[120:121], v[86:87], v[120:121] op_sel:[1,0]
	v_pk_mul_f32 v[92:93], v[86:87], v[92:93] op_sel:[1,0]
	v_lshlrev_b32_e32 v122, 16, v94
	v_and_b32_e32 v123, 0xffff0000, v94
	v_lshlrev_b32_e32 v94, 16, v95
	v_and_b32_e32 v95, 0xffff0000, v95
	v_lshlrev_b32_e32 v126, 16, v98
	v_and_b32_e32 v127, 0xffff0000, v98
	v_lshlrev_b32_e32 v98, 16, v99
	v_and_b32_e32 v99, 0xffff0000, v99
	v_lshlrev_b32_e32 v130, 16, v102
	v_and_b32_e32 v131, 0xffff0000, v102
	v_lshlrev_b32_e32 v102, 16, v103
	v_and_b32_e32 v103, 0xffff0000, v103
	v_lshlrev_b32_e32 v134, 16, v106
	v_and_b32_e32 v135, 0xffff0000, v106
	v_lshlrev_b32_e32 v106, 16, v107
	v_and_b32_e32 v107, 0xffff0000, v107
	v_lshlrev_b32_e32 v138, 16, v110
	v_and_b32_e32 v139, 0xffff0000, v110
	v_lshlrev_b32_e32 v110, 16, v111
	v_and_b32_e32 v111, 0xffff0000, v111
	v_lshlrev_b32_e32 v142, 16, v114
	v_and_b32_e32 v143, 0xffff0000, v114
	v_lshlrev_b32_e32 v114, 16, v115
	v_and_b32_e32 v115, 0xffff0000, v115
	v_lshlrev_b32_e32 v146, 16, v118
	v_and_b32_e32 v147, 0xffff0000, v118
	v_lshlrev_b32_e32 v118, 16, v119
	v_and_b32_e32 v119, 0xffff0000, v119
	v_pk_mul_f32 v[124:125], v[86:87], v[124:125] op_sel:[1,0]
	v_pk_mul_f32 v[96:97], v[86:87], v[96:97] op_sel:[1,0]
	v_pk_mul_f32 v[128:129], v[86:87], v[128:129] op_sel:[1,0]
	v_pk_mul_f32 v[100:101], v[86:87], v[100:101] op_sel:[1,0]
	v_pk_mul_f32 v[132:133], v[86:87], v[132:133] op_sel:[1,0]
	v_pk_mul_f32 v[104:105], v[86:87], v[104:105] op_sel:[1,0]
	v_pk_mul_f32 v[136:137], v[86:87], v[136:137] op_sel:[1,0]
	v_pk_mul_f32 v[108:109], v[86:87], v[108:109] op_sel:[1,0]
	v_pk_mul_f32 v[140:141], v[86:87], v[140:141] op_sel:[1,0]
	v_pk_mul_f32 v[112:113], v[86:87], v[112:113] op_sel:[1,0]
	v_pk_mul_f32 v[144:145], v[86:87], v[144:145] op_sel:[1,0]
	v_pk_mul_f32 v[116:117], v[86:87], v[116:117] op_sel:[1,0]
	v_pk_mul_f32 v[148:149], v[86:87], v[148:149] op_sel:[1,0]
	v_pk_mul_f32 v[50:51], v[86:87], v[50:51] op_sel:[1,0]
	v_pk_fma_f32 v[84:85], v[86:87], v[84:85], v[120:121] op_sel_hi:[0,1,1]
	v_pk_fma_f32 v[90:91], v[86:87], v[90:91], v[92:93] op_sel_hi:[0,1,1]
	v_pk_fma_f32 v[92:93], v[86:87], v[122:123], v[124:125] op_sel_hi:[0,1,1]
	v_pk_fma_f32 v[94:95], v[86:87], v[94:95], v[96:97] op_sel_hi:[0,1,1]
	v_pk_fma_f32 v[96:97], v[86:87], v[126:127], v[128:129] op_sel_hi:[0,1,1]
	v_pk_fma_f32 v[98:99], v[86:87], v[98:99], v[100:101] op_sel_hi:[0,1,1]
	v_pk_fma_f32 v[100:101], v[86:87], v[130:131], v[132:133] op_sel_hi:[0,1,1]
	v_pk_fma_f32 v[102:103], v[86:87], v[102:103], v[104:105] op_sel_hi:[0,1,1]
	v_pk_fma_f32 v[104:105], v[86:87], v[134:135], v[136:137] op_sel_hi:[0,1,1]
	v_pk_fma_f32 v[106:107], v[86:87], v[106:107], v[108:109] op_sel_hi:[0,1,1]
	v_pk_fma_f32 v[108:109], v[86:87], v[138:139], v[140:141] op_sel_hi:[0,1,1]
	v_pk_fma_f32 v[110:111], v[86:87], v[110:111], v[112:113] op_sel_hi:[0,1,1]
	v_pk_fma_f32 v[112:113], v[86:87], v[142:143], v[144:145] op_sel_hi:[0,1,1]
	v_pk_fma_f32 v[114:115], v[86:87], v[114:115], v[116:117] op_sel_hi:[0,1,1]
	v_pk_fma_f32 v[116:117], v[86:87], v[146:147], v[148:149] op_sel_hi:[0,1,1]
	v_pk_fma_f32 v[50:51], v[86:87], v[118:119], v[50:51] op_sel_hi:[0,1,1]
	v_pk_fma_f32 v[0:1], v[180:181], v[84:85], v[88:89]
	v_pk_fma_f32 v[2:3], v[182:183], v[90:91], v[56:57]
	v_pk_fma_f32 v[4:5], v[176:177], v[92:93], v[58:59]
	v_pk_fma_f32 v[6:7], v[178:179], v[94:95], v[60:61]
	v_pk_fma_f32 v[8:9], v[172:173], v[96:97], v[62:63]
	v_pk_fma_f32 v[10:11], v[174:175], v[98:99], v[64:65]
	v_pk_fma_f32 v[12:13], v[168:169], v[100:101], v[66:67]
	v_pk_fma_f32 v[14:15], v[170:171], v[102:103], v[68:69]
	v_pk_fma_f32 v[16:17], v[164:165], v[104:105], v[70:71]
	v_pk_fma_f32 v[18:19], v[166:167], v[106:107], v[72:73]
	v_pk_fma_f32 v[20:21], v[160:161], v[108:109], v[74:75]
	v_pk_fma_f32 v[22:23], v[162:163], v[110:111], v[76:77]
	v_pk_fma_f32 v[24:25], v[156:157], v[112:113], v[78:79]
	v_pk_fma_f32 v[26:27], v[158:159], v[114:115], v[80:81]
	v_pk_fma_f32 v[28:29], v[152:153], v[116:117], v[82:83]
	v_pk_fma_f32 v[30:31], v[154:155], v[50:51], v[48:49]
	global_store_dwordx4 v[52:53], v[0:3], off offset:-3072
	global_store_dwordx4 v[52:53], v[4:7], off offset:-2048
	global_store_dwordx4 v[52:53], v[8:11], off offset:-1024
	global_store_dwordx4 v[46:47], v[12:15], off offset:-4096
	global_store_dwordx4 v[46:47], v[16:19], off offset:-3072
	global_store_dwordx4 v[46:47], v[20:23], off offset:-2048
	global_store_dwordx4 v[46:47], v[24:27], off offset:-1024
	global_store_dwordx4 v[46:47], v[28:31], off
	v_lshl_add_u64 v[46:47], v[46:47], 0, s[2:3]
	s_cbranch_scc1 .LBB0_2857
